# v16
# speedup vs baseline: 1.0198x; 1.0197x over previous
.LBB1_3:
	v_lshrrev_b32_e32 v3, 4, v0
	v_and_b32_e32 v4, 15, v0
	v_bfe_u32 v5, v0, 4, 2
	v_and_b32_e32 v7, 7, v0
	s_lshl_b32 s0, s30, 5
	s_sext_i32_i16 s76, s28
	v_lshl_or_b32 v207, s31, 6, v4
	v_bitop3_b32 v3, v3, v7, 3 bitop3:0x6c
	v_bitop3_b32 v7, v5, v7, 4 bitop3:0x36
	s_and_b32 s28, s0, 0x60
	v_lshlrev_b32_e32 v6, 7, v207
	v_lshlrev_b32_e32 v3, 4, v3
	v_lshlrev_b32_e32 v7, 4, v7
	v_or_b32_e32 v4, s28, v4
	s_cmp_lg_u32 s16, 0
	v_lshlrev_b32_e32 v206, 2, v0
	v_lshlrev_b32_e32 v0, 4, v0
	v_or_b32_e32 v8, v6, v3
	v_or_b32_e32 v6, v6, v7
	v_lshlrev_b32_e32 v4, 7, v4
	s_cselect_b64 s[0:1], -1, 0
	v_add_u32_e32 v208, v2, v1
	v_add_u32_e32 v0, 0, v0
	v_or_b32_e32 v222, v4, v3
	v_or_b32_e32 v223, v4, v7
	v_add_u32_e32 v228, 0x10000, v222
	v_add_u32_e32 v229, 0x10000, v223
	s_mul_i32 s65, s2, 0x70
	v_lshl_or_b32 v224, v5, 3, s28
	v_add_u32_e32 v210, 0x80000, v208
	v_mov_b32_e32 v211, v205
	v_mov_b32_e32 v209, v205
	s_and_b64 s[0:1], exec, s[0:1]
	s_movk_i32 s16, 0xe00
	v_add_u32_e32 v225, 0x20000, v0
	s_add_i32 s66, 0, 0x10000
	s_add_i32 s67, 0, 0x10800
	s_add_i32 s68, 0, 0x14000
	s_add_i32 s69, 0, 0x14800
	s_add_i32 s70, 0, 0x18000
	s_add_i32 s71, 0, 0x18800
	s_add_i32 s72, 0, 0x1c000
	s_add_i32 s73, 0, 0x1c800
	s_movk_i32 s74, 0x7000
	v_add_u32_e32 v226, 0, v8
	v_add_u32_e32 v227, 0, v6
	s_mov_b32 s30, s29
	s_mov_b32 s34, s29
	s_mov_b32 s28, 0
	s_branch .LBB1_5

.LBB1_14:
	ds_read_b128 v[148:151], v228
	ds_read_b128 v[152:155], v229
	ds_read_b128 v[156:159], v228 offset:2048
	ds_read_b128 v[160:163], v229 offset:2048
	s_add_i32 m0, s43, 0xc000
	ds_read_b128 v[132:135], v228 offset:16384
	ds_read_b128 v[136:139], v229 offset:16384
	ds_read_b128 v[140:143], v228 offset:18432
	ds_read_b128 v[144:147], v229 offset:18432
	ds_read_b128 v[166:169], v226
	ds_read_b128 v[170:173], v226 offset:2048
	ds_read_b128 v[174:177], v227
	ds_read_b128 v[178:181], v227 offset:2048
	ds_read_b128 v[182:185], v226 offset:4096
	ds_read_b128 v[186:189], v226 offset:6144
	ds_read_b128 v[190:193], v227 offset:4096
	ds_read_b128 v[214:217], v227 offset:6144
	global_load_lds_dwordx4 v208, s[44:45]
	s_add_i32 m0, s43, 0xe000
	s_nop 0
	global_load_lds_dwordx4 v210, s[44:45]
	s_waitcnt vmcnt(8)
	s_waitcnt lgkmcnt(0)
	s_barrier
	s_setprio 1
	s_waitcnt lgkmcnt(0)
	v_mfma_f32_16x16x32_f16 v[128:131], v[148:151], v[166:169], v[128:131]
	v_mfma_f32_16x16x32_f16 v[128:131], v[152:155], v[174:177], v[128:131]
	v_mfma_f32_16x16x32_f16 v[120:123], v[160:163], v[174:177], v[120:123]
	v_mfma_f32_16x16x32_f16 v[120:123], v[156:159], v[166:169], v[120:123]
	v_mfma_f32_16x16x32_f16 v[104:107], v[156:159], v[170:173], v[104:107]
	v_mfma_f32_16x16x32_f16 v[104:107], v[160:163], v[178:181], v[104:107]
	v_mfma_f32_16x16x32_f16 v[112:115], v[152:155], v[178:181], v[112:115]
	v_mfma_f32_16x16x32_f16 v[112:115], v[148:151], v[170:173], v[112:115]
	v_mfma_f32_16x16x32_f16 v[96:99], v[148:151], v[182:185], v[96:99]
	v_mfma_f32_16x16x32_f16 v[96:99], v[152:155], v[190:193], v[96:99]
	v_mfma_f32_16x16x32_f16 v[88:91], v[160:163], v[190:193], v[88:91]
	v_mfma_f32_16x16x32_f16 v[88:91], v[156:159], v[182:185], v[88:91]
	v_mfma_f32_16x16x32_f16 v[72:75], v[156:159], v[186:189], v[72:75]
	v_mfma_f32_16x16x32_f16 v[72:75], v[160:163], v[214:217], v[72:75]
	v_mfma_f32_16x16x32_f16 v[80:83], v[152:155], v[214:217], v[80:83]
	v_mfma_f32_16x16x32_f16 v[80:83], v[148:151], v[186:189], v[80:83]
	s_setprio 0
	s_setprio 1
	v_mfma_f32_16x16x32_f16 v[124:127], v[132:135], v[166:169], v[124:127]
	v_mfma_f32_16x16x32_f16 v[124:127], v[136:139], v[174:177], v[124:127]
	v_mfma_f32_16x16x32_f16 v[116:119], v[144:147], v[174:177], v[116:119]
	v_mfma_f32_16x16x32_f16 v[116:119], v[140:143], v[166:169], v[116:119]
	v_mfma_f32_16x16x32_f16 v[100:103], v[140:143], v[170:173], v[100:103]
	v_mfma_f32_16x16x32_f16 v[100:103], v[144:147], v[178:181], v[100:103]
	v_mfma_f32_16x16x32_f16 v[108:111], v[136:139], v[178:181], v[108:111]
	v_mfma_f32_16x16x32_f16 v[108:111], v[132:135], v[170:173], v[108:111]
	v_mfma_f32_16x16x32_f16 v[92:95], v[132:135], v[182:185], v[92:95]
	v_mfma_f32_16x16x32_f16 v[92:95], v[136:139], v[190:193], v[92:95]
	v_mfma_f32_16x16x32_f16 v[84:87], v[144:147], v[190:193], v[84:87]
	v_mfma_f32_16x16x32_f16 v[84:87], v[140:143], v[182:185], v[84:87]
	v_mfma_f32_16x16x32_f16 v[68:71], v[140:143], v[186:189], v[68:71]
	v_mfma_f32_16x16x32_f16 v[68:71], v[144:147], v[214:217], v[68:71]
	v_mfma_f32_16x16x32_f16 v[76:79], v[136:139], v[214:217], v[76:79]
	v_mfma_f32_16x16x32_f16 v[76:79], v[132:135], v[186:189], v[76:79]
	s_setprio 0
	s_barrier
	s_andn2_b64 vcc, exec, s[4:5]
	s_cbranch_vccnz .LBB1_16
	v_cvt_pkrtz_f16_f32 v166, v0, v1
	v_cvt_pkrtz_f16_f32 v167, v2, v3
	v_add_u32_e32 v166, 0x20002, v166
	v_add_u32_e32 v167, 0x20002, v167
	v_and_b32_e32 v166, 0xfffcfffc, v166
	v_and_b32_e32 v167, 0xfffcfffc, v167
	global_store_dwordx2 v[164:165], v[166:167], off
.LBB1_16:
	s_add_u32 s28, s44, 0xfff00080
	s_addc_u32 s46, s45, -1
	s_cmp_eq_u32 s48, 60
	s_cselect_b32 s49, s31, s46
	s_cselect_b32 s47, s35, s81
	s_cselect_b32 s46, s78, s80
	s_mov_b32 m0, s52
	s_cselect_b32 s48, s77, s28
	s_add_u32 s50, s46, 0x100000
	ds_read_b128 v[188:191], v226 offset:16384
	ds_read_b128 v[176:179], v226 offset:18432
	ds_read_b128 v[192:195], v227 offset:16384
	ds_read_b128 v[180:183], v227 offset:18432
	ds_read_b128 v[172:175], v226 offset:20480
	ds_read_b128 v[164:167], v226 offset:22528
	ds_read_b128 v[184:187], v227 offset:20480
	ds_read_b128 v[168:171], v227 offset:22528
	global_load_lds_dwordx4 v200, s[46:47]
	s_mov_b32 m0, s53
	s_addc_u32 s51, s47, 0
	global_load_lds_dwordx4 v196, s[46:47]
	s_mov_b32 m0, s55
	s_add_u32 s84, s46, 0x80
	s_addc_u32 s85, s47, 0
	global_load_lds_dwordx4 v200, s[50:51]
	s_mov_b32 m0, s56
	s_add_u32 s86, s48, 0x80
	s_addc_u32 s87, s49, 0
	s_and_b64 s[4:5], exec, s[4:5]
	global_load_lds_dwordx4 v196, s[50:51]
	s_mov_b32 m0, s43
	s_mov_b64 s[50:51], -1
	global_load_lds_dwordx4 v202, s[48:49]
	s_mov_b32 m0, s54
	s_mov_b64 vcc, s[4:5]
	global_load_lds_dwordx4 v198, s[48:49]
	s_cbranch_vccz .LBB1_18
	s_waitcnt vmcnt(8)
	s_mov_b64 s[50:51], 0

.LBB1_20:
	s_waitcnt lgkmcnt(0)
	s_barrier
	s_setprio 1
	s_waitcnt lgkmcnt(0)
	v_mfma_f32_16x16x32_f16 v[64:67], v[148:151], v[188:191], v[64:67]
	v_mfma_f32_16x16x32_f16 v[64:67], v[152:155], v[192:195], v[64:67]
	v_mfma_f32_16x16x32_f16 v[56:59], v[160:163], v[192:195], v[56:59]
	v_mfma_f32_16x16x32_f16 v[56:59], v[156:159], v[188:191], v[56:59]
	v_mfma_f32_16x16x32_f16 v[40:43], v[156:159], v[176:179], v[40:43]
	v_mfma_f32_16x16x32_f16 v[40:43], v[160:163], v[180:183], v[40:43]
	v_mfma_f32_16x16x32_f16 v[48:51], v[152:155], v[180:183], v[48:51]
	v_mfma_f32_16x16x32_f16 v[48:51], v[148:151], v[176:179], v[48:51]
	v_mfma_f32_16x16x32_f16 v[32:35], v[148:151], v[172:175], v[32:35]
	v_mfma_f32_16x16x32_f16 v[32:35], v[152:155], v[184:187], v[32:35]
	v_mfma_f32_16x16x32_f16 v[24:27], v[160:163], v[184:187], v[24:27]
	v_mfma_f32_16x16x32_f16 v[24:27], v[156:159], v[172:175], v[24:27]
	v_mfma_f32_16x16x32_f16 v[8:11], v[156:159], v[164:167], v[8:11]
	v_mfma_f32_16x16x32_f16 v[8:11], v[160:163], v[168:171], v[8:11]
	v_mfma_f32_16x16x32_f16 v[16:19], v[152:155], v[168:171], v[16:19]
	v_mfma_f32_16x16x32_f16 v[16:19], v[148:151], v[164:167], v[16:19]
	s_setprio 0
	s_setprio 1
	v_mfma_f32_16x16x32_f16 v[60:63], v[132:135], v[188:191], v[60:63]
	v_mfma_f32_16x16x32_f16 v[60:63], v[136:139], v[192:195], v[60:63]
	v_mfma_f32_16x16x32_f16 v[52:55], v[144:147], v[192:195], v[52:55]
	v_mfma_f32_16x16x32_f16 v[52:55], v[140:143], v[188:191], v[52:55]
	v_mfma_f32_16x16x32_f16 v[36:39], v[140:143], v[176:179], v[36:39]
	v_mfma_f32_16x16x32_f16 v[36:39], v[144:147], v[180:183], v[36:39]
	v_mfma_f32_16x16x32_f16 v[44:47], v[136:139], v[180:183], v[44:47]
	v_mfma_f32_16x16x32_f16 v[44:47], v[132:135], v[176:179], v[44:47]
	v_mfma_f32_16x16x32_f16 v[28:31], v[132:135], v[172:175], v[28:31]
	v_mfma_f32_16x16x32_f16 v[28:31], v[136:139], v[184:187], v[28:31]
	v_mfma_f32_16x16x32_f16 v[20:23], v[144:147], v[184:187], v[20:23]
	v_mfma_f32_16x16x32_f16 v[20:23], v[140:143], v[172:175], v[20:23]
	v_mfma_f32_16x16x32_f16 v[4:7], v[140:143], v[164:167], v[4:7]
	v_mfma_f32_16x16x32_f16 v[4:7], v[144:147], v[168:171], v[4:7]
	v_mfma_f32_16x16x32_f16 v[12:15], v[136:139], v[168:171], v[12:15]
	v_mfma_f32_16x16x32_f16 v[12:15], v[132:135], v[164:167], v[12:15]
	s_setprio 0
	s_barrier
	s_add_u32 s48, s48, 0x100000
	ds_read_b128 v[148:151], v228 offset:32768
	ds_read_b128 v[152:155], v229 offset:32768
	s_addc_u32 s49, s49, 0
	s_mov_b32 m0, s57
	ds_read_b128 v[156:159], v228 offset:34816
	ds_read_b128 v[160:163], v229 offset:34816
	ds_read_b128 v[132:135], v228 offset:49152
	ds_read_b128 v[136:139], v229 offset:49152
	ds_read_b128 v[140:143], v228 offset:51200
	ds_read_b128 v[144:147], v229 offset:51200
	ds_read_b128 v[188:191], v226 offset:32768
	ds_read_b128 v[176:179], v226 offset:34816
	ds_read_b128 v[192:195], v227 offset:32768
	ds_read_b128 v[180:183], v227 offset:34816
	ds_read_b128 v[172:175], v226 offset:36864
	ds_read_b128 v[164:167], v226 offset:38912
	ds_read_b128 v[184:187], v227 offset:36864
	ds_read_b128 v[168:171], v227 offset:38912
	global_load_lds_dwordx4 v202, s[48:49]
	s_mov_b32 m0, s58
	s_nop 0
	global_load_lds_dwordx4 v198, s[48:49]
	s_mov_b64 s[48:49], -1
	s_mov_b64 vcc, s[4:5]
	s_cbranch_vccz .LBB1_22
	s_waitcnt vmcnt(8)
	s_mov_b64 s[48:49], 0

.LBB1_24:
	s_waitcnt lgkmcnt(0)
	s_barrier
	s_setprio 1
	s_waitcnt lgkmcnt(0)
	v_mfma_f32_16x16x32_f16 v[128:131], v[148:151], v[188:191], v[128:131]
	v_mfma_f32_16x16x32_f16 v[128:131], v[152:155], v[192:195], v[128:131]
	v_mfma_f32_16x16x32_f16 v[120:123], v[160:163], v[192:195], v[120:123]
	v_mfma_f32_16x16x32_f16 v[120:123], v[156:159], v[188:191], v[120:123]
	v_mfma_f32_16x16x32_f16 v[104:107], v[156:159], v[176:179], v[104:107]
	v_mfma_f32_16x16x32_f16 v[104:107], v[160:163], v[180:183], v[104:107]
	v_mfma_f32_16x16x32_f16 v[112:115], v[152:155], v[180:183], v[112:115]
	v_mfma_f32_16x16x32_f16 v[112:115], v[148:151], v[176:179], v[112:115]
	v_mfma_f32_16x16x32_f16 v[96:99], v[148:151], v[172:175], v[96:99]
	v_mfma_f32_16x16x32_f16 v[96:99], v[152:155], v[184:187], v[96:99]
	v_mfma_f32_16x16x32_f16 v[88:91], v[160:163], v[184:187], v[88:91]
	v_mfma_f32_16x16x32_f16 v[88:91], v[156:159], v[172:175], v[88:91]
	v_mfma_f32_16x16x32_f16 v[72:75], v[156:159], v[164:167], v[72:75]
	v_mfma_f32_16x16x32_f16 v[72:75], v[160:163], v[168:171], v[72:75]
	v_mfma_f32_16x16x32_f16 v[80:83], v[152:155], v[168:171], v[80:83]
	v_mfma_f32_16x16x32_f16 v[80:83], v[148:151], v[164:167], v[80:83]
	s_setprio 0
	s_setprio 1
	v_mfma_f32_16x16x32_f16 v[124:127], v[132:135], v[188:191], v[124:127]
	v_mfma_f32_16x16x32_f16 v[124:127], v[136:139], v[192:195], v[124:127]
	v_mfma_f32_16x16x32_f16 v[116:119], v[144:147], v[192:195], v[116:119]
	v_mfma_f32_16x16x32_f16 v[116:119], v[140:143], v[188:191], v[116:119]
	v_mfma_f32_16x16x32_f16 v[100:103], v[140:143], v[176:179], v[100:103]
	v_mfma_f32_16x16x32_f16 v[100:103], v[144:147], v[180:183], v[100:103]
	v_mfma_f32_16x16x32_f16 v[108:111], v[136:139], v[180:183], v[108:111]
	v_mfma_f32_16x16x32_f16 v[108:111], v[132:135], v[176:179], v[108:111]
	v_mfma_f32_16x16x32_f16 v[92:95], v[132:135], v[172:175], v[92:95]
	v_mfma_f32_16x16x32_f16 v[92:95], v[136:139], v[184:187], v[92:95]
	v_mfma_f32_16x16x32_f16 v[84:87], v[144:147], v[184:187], v[84:87]
	v_mfma_f32_16x16x32_f16 v[84:87], v[140:143], v[172:175], v[84:87]
	v_mfma_f32_16x16x32_f16 v[68:71], v[140:143], v[164:167], v[68:71]
	v_mfma_f32_16x16x32_f16 v[68:71], v[144:147], v[168:171], v[68:71]
	v_mfma_f32_16x16x32_f16 v[76:79], v[136:139], v[168:171], v[76:79]
	v_mfma_f32_16x16x32_f16 v[76:79], v[132:135], v[164:167], v[76:79]
	s_setprio 0
	s_barrier
	s_mov_b32 m0, s59
	s_add_u32 s4, s46, 0x100080
	ds_read_b128 v[164:167], v226 offset:49152
	ds_read_b128 v[168:171], v226 offset:51200
	ds_read_b128 v[172:175], v227 offset:49152
	ds_read_b128 v[176:179], v227 offset:51200
	ds_read_b128 v[180:183], v226 offset:53248
	ds_read_b128 v[184:187], v226 offset:55296
	ds_read_b128 v[188:191], v227 offset:53248
	ds_read_b128 v[192:195], v227 offset:55296
	global_load_lds_dwordx4 v200, s[84:85]
	s_mov_b32 m0, s60
	s_addc_u32 s5, s47, 0
	global_load_lds_dwordx4 v196, s[84:85]
	s_mov_b32 m0, s63
	s_nop 0
	global_load_lds_dwordx4 v200, s[4:5]
	s_mov_b32 m0, s64
	s_nop 0
	global_load_lds_dwordx4 v196, s[4:5]
	s_mov_b32 m0, s61
	s_nop 0
	global_load_lds_dwordx4 v202, s[86:87]
	s_mov_b32 m0, s62
	s_nop 0
	global_load_lds_dwordx4 v198, s[86:87]
	s_waitcnt vmcnt(8)
	s_waitcnt lgkmcnt(0)
	s_barrier
	s_setprio 1
	s_waitcnt lgkmcnt(0)
	v_mfma_f32_16x16x32_f16 v[64:67], v[148:151], v[164:167], v[64:67]
	v_mfma_f32_16x16x32_f16 v[64:67], v[152:155], v[172:175], v[64:67]
	v_mfma_f32_16x16x32_f16 v[56:59], v[160:163], v[172:175], v[56:59]
	v_mfma_f32_16x16x32_f16 v[56:59], v[156:159], v[164:167], v[56:59]
	v_mfma_f32_16x16x32_f16 v[40:43], v[156:159], v[168:171], v[40:43]
	v_mfma_f32_16x16x32_f16 v[40:43], v[160:163], v[176:179], v[40:43]
	v_mfma_f32_16x16x32_f16 v[48:51], v[152:155], v[176:179], v[48:51]
	v_mfma_f32_16x16x32_f16 v[48:51], v[148:151], v[168:171], v[48:51]
	v_mfma_f32_16x16x32_f16 v[32:35], v[148:151], v[180:183], v[32:35]
	v_mfma_f32_16x16x32_f16 v[32:35], v[152:155], v[188:191], v[32:35]
	v_mfma_f32_16x16x32_f16 v[24:27], v[160:163], v[188:191], v[24:27]
	v_mfma_f32_16x16x32_f16 v[24:27], v[156:159], v[180:183], v[24:27]
	v_mfma_f32_16x16x32_f16 v[8:11], v[156:159], v[184:187], v[8:11]
	v_mfma_f32_16x16x32_f16 v[8:11], v[160:163], v[192:195], v[8:11]
	v_mfma_f32_16x16x32_f16 v[16:19], v[152:155], v[192:195], v[16:19]
	v_mfma_f32_16x16x32_f16 v[16:19], v[148:151], v[184:187], v[16:19]
	s_setprio 0
	s_setprio 1
	v_mfma_f32_16x16x32_f16 v[60:63], v[132:135], v[164:167], v[60:63]
	v_mfma_f32_16x16x32_f16 v[60:63], v[136:139], v[172:175], v[60:63]
	v_mfma_f32_16x16x32_f16 v[52:55], v[144:147], v[172:175], v[52:55]
	v_mfma_f32_16x16x32_f16 v[52:55], v[140:143], v[164:167], v[52:55]
	v_mfma_f32_16x16x32_f16 v[36:39], v[140:143], v[168:171], v[36:39]
	v_mfma_f32_16x16x32_f16 v[36:39], v[144:147], v[176:179], v[36:39]
	v_mfma_f32_16x16x32_f16 v[44:47], v[136:139], v[176:179], v[44:47]
	v_mfma_f32_16x16x32_f16 v[44:47], v[132:135], v[168:171], v[44:47]
	v_mfma_f32_16x16x32_f16 v[28:31], v[132:135], v[180:183], v[28:31]
	v_mfma_f32_16x16x32_f16 v[28:31], v[136:139], v[188:191], v[28:31]
	v_mfma_f32_16x16x32_f16 v[20:23], v[144:147], v[188:191], v[20:23]
	v_mfma_f32_16x16x32_f16 v[20:23], v[140:143], v[180:183], v[20:23]
	v_mfma_f32_16x16x32_f16 v[4:7], v[140:143], v[184:187], v[4:7]
	v_mfma_f32_16x16x32_f16 v[4:7], v[144:147], v[192:195], v[4:7]
	v_mfma_f32_16x16x32_f16 v[12:15], v[136:139], v[192:195], v[12:15]
	v_mfma_f32_16x16x32_f16 v[12:15], v[132:135], v[184:187], v[12:15]
	s_setprio 0
	s_barrier
	s_add_u32 s80, s80, 0x100
	s_addc_u32 s81, s81, 0
	s_add_u32 s44, s44, 0x100
	s_addc_u32 s45, s45, 0
	s_cmp_gt_u32 s82, 61
	s_cbranch_scc1 .LBB1_4
	s_mov_b32 s48, s82
	s_branch .LBB1_9

.LBB1_30:
	s_endpgm
	s_nop 0
	s_nop 0
	s_nop 0
	s_nop 0
	s_nop 0
	s_nop 0
	s_nop 0
	s_nop 0
	s_nop 0
	s_nop 0
	s_nop 0
	s_nop 0
	s_nop 0
	s_nop 0
	s_nop 0
	s_nop 0
	s_nop 0
	s_nop 0
	s_nop 0
	s_nop 0
	s_nop 0
	s_nop 0
	s_nop 0
	s_nop 0
	s_nop 0
	s_nop 0
	s_nop 0
	s_nop 0
	s_nop 0
	s_nop 0
	s_nop 0
	s_nop 0
	s_nop 0
	s_nop 0
	s_nop 0
	s_nop 0
	s_nop 0
	s_nop 0
	s_nop 0
	s_nop 0
	s_nop 0
	s_nop 0
	s_nop 0
	s_nop 0
	s_nop 0
	s_nop 0
	s_nop 0
	s_nop 0
	s_nop 0
	s_nop 0
	s_endpgm

	.amdhsa_kernel _Z12gemm_persistILi0ELi4096ELi32ELi112EEvPKDF16_S1_PvPKfS4_S4_S4_PDF16_S5_iii
		.amdhsa_group_segment_fixed_size 0
		.amdhsa_private_segment_fixed_size 0
		.amdhsa_kernarg_size 344
		.amdhsa_user_sgpr_count 2
		.amdhsa_user_sgpr_dispatch_ptr 0
		.amdhsa_user_sgpr_queue_ptr 0
		.amdhsa_user_sgpr_kernarg_segment_ptr 1
		.amdhsa_user_sgpr_dispatch_id 0
		.amdhsa_user_sgpr_kernarg_preload_length 0
		.amdhsa_user_sgpr_kernarg_preload_offset 0
		.amdhsa_user_sgpr_private_segment_size 0
		.amdhsa_uses_dynamic_stack 0
		.amdhsa_enable_private_segment 0
		.amdhsa_system_sgpr_workgroup_id_x 1
		.amdhsa_system_sgpr_workgroup_id_y 0
		.amdhsa_system_sgpr_workgroup_id_z 0
		.amdhsa_system_sgpr_workgroup_info 0
		.amdhsa_system_vgpr_workitem_id 0
		.amdhsa_next_free_vgpr 232
		.amdhsa_next_free_sgpr 88
		.amdhsa_accum_offset 232
		.amdhsa_reserve_vcc 1
		.amdhsa_float_round_mode_32 0
		.amdhsa_float_round_mode_16_64 0
		.amdhsa_float_denorm_mode_32 3
		.amdhsa_float_denorm_mode_16_64 3
		.amdhsa_dx10_clamp 1
		.amdhsa_ieee_mode 1
		.amdhsa_fp16_overflow 0
		.amdhsa_tg_split 0
		.amdhsa_exception_fp_ieee_invalid_op 0
		.amdhsa_exception_fp_denorm_src 0
		.amdhsa_exception_fp_ieee_div_zero 0
		.amdhsa_exception_fp_ieee_overflow 0
		.amdhsa_exception_fp_ieee_underflow 0
		.amdhsa_exception_fp_ieee_inexact 0
		.amdhsa_exception_int_div_zero 0
	.end_amdhsa_kernel

.LBB2_20:
	s_add_u32 s30, s28, 0xffc80080
	s_addc_u32 s31, s29, -1
	s_cmpk_eq_i32 s58, 0xdc
	s_cselect_b32 s35, s25, s31
	s_cselect_b32 s34, s24, s30
	s_cselect_b32 s31, s27, s57
	s_cselect_b32 s30, s26, s56
	s_add_i32 m0, s37, 0xc000
	ds_read_b128 v[166:169], v143
	ds_read_b128 v[170:173], v147
	ds_read_b128 v[174:177], v149
	ds_read_b128 v[178:181], v150
	ds_read_b128 v[182:185], v151
	ds_read_b128 v[186:189], v152
	ds_read_b128 v[190:193], v153
	ds_read_b128 v[194:197], v154
	ds_read_b128 v[198:201], v155
	ds_read_b128 v[202:205], v155 offset:2048
	ds_read_b128 v[206:209], v156
	ds_read_b128 v[210:213], v156 offset:2048
	ds_read_b128 v[214:217], v155 offset:4096
	ds_read_b128 v[218:221], v155 offset:6144
	ds_read_b128 v[222:225], v156 offset:4096
	ds_read_b128 v[226:229], v156 offset:6144
	global_load_lds_dwordx4 v134, s[28:29]
	s_add_i32 m0, s37, 0xe000
	s_nop 0
	global_load_lds_dwordx4 v132, s[28:29]
	s_waitcnt vmcnt(8)
	s_waitcnt lgkmcnt(0)
	s_barrier
	s_setprio 1
	s_waitcnt lgkmcnt(0)
	v_mfma_f32_16x16x32_f16 v[124:127], v[166:169], v[198:201], v[124:127]
	v_mfma_f32_16x16x32_f16 v[124:127], v[170:173], v[206:209], v[124:127]
	v_mfma_f32_16x16x32_f16 v[120:123], v[178:181], v[206:209], v[120:123]
	v_mfma_f32_16x16x32_f16 v[120:123], v[174:177], v[198:201], v[120:123]
	v_mfma_f32_16x16x32_f16 v[112:115], v[174:177], v[202:205], v[112:115]
	v_mfma_f32_16x16x32_f16 v[112:115], v[178:181], v[210:213], v[112:115]
	v_mfma_f32_16x16x32_f16 v[116:119], v[170:173], v[210:213], v[116:119]
	v_mfma_f32_16x16x32_f16 v[116:119], v[166:169], v[202:205], v[116:119]
	v_mfma_f32_16x16x32_f16 v[108:111], v[166:169], v[214:217], v[108:111]
	v_mfma_f32_16x16x32_f16 v[108:111], v[170:173], v[222:225], v[108:111]
	v_mfma_f32_16x16x32_f16 v[100:103], v[178:181], v[222:225], v[100:103]
	v_mfma_f32_16x16x32_f16 v[100:103], v[174:177], v[214:217], v[100:103]
	v_mfma_f32_16x16x32_f16 v[84:87], v[174:177], v[218:221], v[84:87]
	v_mfma_f32_16x16x32_f16 v[84:87], v[178:181], v[226:229], v[84:87]
	v_mfma_f32_16x16x32_f16 v[92:95], v[170:173], v[226:229], v[92:95]
	v_mfma_f32_16x16x32_f16 v[92:95], v[166:169], v[218:221], v[92:95]
	s_setprio 0
	s_setprio 1
	v_mfma_f32_16x16x32_f16 v[104:107], v[182:185], v[198:201], v[104:107]
	v_mfma_f32_16x16x32_f16 v[104:107], v[186:189], v[206:209], v[104:107]
	v_mfma_f32_16x16x32_f16 v[96:99], v[194:197], v[206:209], v[96:99]
	v_mfma_f32_16x16x32_f16 v[96:99], v[190:193], v[198:201], v[96:99]
	v_mfma_f32_16x16x32_f16 v[80:83], v[190:193], v[202:205], v[80:83]
	v_mfma_f32_16x16x32_f16 v[80:83], v[194:197], v[210:213], v[80:83]
	v_mfma_f32_16x16x32_f16 v[88:91], v[186:189], v[210:213], v[88:91]
	v_mfma_f32_16x16x32_f16 v[88:91], v[182:185], v[202:205], v[88:91]
	v_mfma_f32_16x16x32_f16 v[76:79], v[182:185], v[214:217], v[76:79]
	v_mfma_f32_16x16x32_f16 v[76:79], v[186:189], v[222:225], v[76:79]
	v_mfma_f32_16x16x32_f16 v[72:75], v[194:197], v[222:225], v[72:75]
	v_mfma_f32_16x16x32_f16 v[72:75], v[190:193], v[214:217], v[72:75]
	v_mfma_f32_16x16x32_f16 v[64:67], v[190:193], v[218:221], v[64:67]
	v_mfma_f32_16x16x32_f16 v[64:67], v[194:197], v[226:229], v[64:67]
	v_mfma_f32_16x16x32_f16 v[68:71], v[186:189], v[226:229], v[68:71]
	v_mfma_f32_16x16x32_f16 v[68:71], v[182:185], v[218:221], v[68:71]
	s_setprio 0
	s_barrier
	s_add_i32 s59, s43, s36
	s_mov_b32 m0, s59
	ds_read_b128 v[198:201], v155 offset:16384
	ds_read_b128 v[202:205], v155 offset:18432
	ds_read_b128 v[206:209], v156 offset:16384
	ds_read_b128 v[210:213], v156 offset:18432
	ds_read_b128 v[214:217], v155 offset:20480
	ds_read_b128 v[218:221], v155 offset:22528
	ds_read_b128 v[222:225], v156 offset:20480
	ds_read_b128 v[226:229], v156 offset:22528
	global_load_lds_dwordx4 v128, s[30:31]
	s_add_i32 m0, s59, 0x2000
	s_add_u32 s60, s30, 0x380000
	s_addc_u32 s61, s31, 0
	s_add_i32 s59, s44, s36
	global_load_lds_dwordx4 v130, s[30:31]
	s_mov_b32 m0, s59
	s_add_u32 s62, s30, 0x80
	s_addc_u32 s63, s31, 0
	global_load_lds_dwordx4 v128, s[60:61]
	s_add_i32 m0, s59, 0x2000
	s_add_u32 s64, s34, 0x80
	s_addc_u32 s65, s35, 0
	global_load_lds_dwordx4 v130, s[60:61]
	s_mov_b32 m0, s37
	s_nop 0
	global_load_lds_dwordx4 v128, s[34:35]
	s_mov_b32 m0, s38
	s_nop 0
	global_load_lds_dwordx4 v130, s[34:35]
	s_waitcnt vmcnt(8)
	s_waitcnt lgkmcnt(0)
	s_barrier
	s_setprio 1
	s_waitcnt lgkmcnt(0)
	v_mfma_f32_16x16x32_f16 v[60:63], v[166:169], v[198:201], v[60:63]
	v_mfma_f32_16x16x32_f16 v[60:63], v[170:173], v[206:209], v[60:63]
	v_mfma_f32_16x16x32_f16 v[56:59], v[178:181], v[206:209], v[56:59]
	v_mfma_f32_16x16x32_f16 v[56:59], v[174:177], v[198:201], v[56:59]
	v_mfma_f32_16x16x32_f16 v[48:51], v[174:177], v[202:205], v[48:51]
	v_mfma_f32_16x16x32_f16 v[48:51], v[178:181], v[210:213], v[48:51]
	v_mfma_f32_16x16x32_f16 v[52:55], v[170:173], v[210:213], v[52:55]
	v_mfma_f32_16x16x32_f16 v[52:55], v[166:169], v[202:205], v[52:55]
	v_mfma_f32_16x16x32_f16 v[40:43], v[166:169], v[214:217], v[40:43]
	v_mfma_f32_16x16x32_f16 v[40:43], v[170:173], v[222:225], v[40:43]
	v_mfma_f32_16x16x32_f16 v[32:35], v[178:181], v[222:225], v[32:35]
	v_mfma_f32_16x16x32_f16 v[32:35], v[174:177], v[214:217], v[32:35]
	v_mfma_f32_16x16x32_f16 v[8:11], v[174:177], v[218:221], v[8:11]
	v_mfma_f32_16x16x32_f16 v[8:11], v[178:181], v[226:229], v[8:11]
	v_mfma_f32_16x16x32_f16 v[12:15], v[170:173], v[226:229], v[12:15]
	v_mfma_f32_16x16x32_f16 v[12:15], v[166:169], v[218:221], v[12:15]
	s_setprio 0
	s_setprio 1
	v_mfma_f32_16x16x32_f16 v[44:47], v[182:185], v[198:201], v[44:47]
	v_mfma_f32_16x16x32_f16 v[44:47], v[186:189], v[206:209], v[44:47]
	v_mfma_f32_16x16x32_f16 v[36:39], v[194:197], v[206:209], v[36:39]
	v_mfma_f32_16x16x32_f16 v[36:39], v[190:193], v[198:201], v[36:39]
	v_mfma_f32_16x16x32_f16 v[24:27], v[190:193], v[202:205], v[24:27]
	v_mfma_f32_16x16x32_f16 v[24:27], v[194:197], v[210:213], v[24:27]
	v_mfma_f32_16x16x32_f16 v[28:31], v[186:189], v[210:213], v[28:31]
	v_mfma_f32_16x16x32_f16 v[28:31], v[182:185], v[202:205], v[28:31]
	v_mfma_f32_16x16x32_f16 v[20:23], v[182:185], v[214:217], v[20:23]
	v_mfma_f32_16x16x32_f16 v[20:23], v[186:189], v[222:225], v[20:23]
	v_mfma_f32_16x16x32_f16 v[16:19], v[194:197], v[222:225], v[16:19]
	v_mfma_f32_16x16x32_f16 v[16:19], v[190:193], v[214:217], v[16:19]
	v_mfma_f32_16x16x32_f16 v[0:3], v[190:193], v[218:221], v[0:3]
	v_mfma_f32_16x16x32_f16 v[0:3], v[194:197], v[226:229], v[0:3]
	v_mfma_f32_16x16x32_f16 v[4:7], v[186:189], v[226:229], v[4:7]
	v_mfma_f32_16x16x32_f16 v[4:7], v[182:185], v[218:221], v[4:7]
	s_setprio 0
	s_barrier
	s_add_u32 s34, s34, 0x380000
	s_addc_u32 s35, s35, 0
	s_mov_b32 m0, s39
	ds_read_b128 v[166:169], v157
	ds_read_b128 v[170:173], v158
	ds_read_b128 v[174:177], v159
	ds_read_b128 v[178:181], v160
	ds_read_b128 v[182:185], v161
	ds_read_b128 v[186:189], v162
	ds_read_b128 v[190:193], v163
	ds_read_b128 v[194:197], v164
	ds_read_b128 v[198:201], v155 offset:32768
	ds_read_b128 v[202:205], v155 offset:34816
	ds_read_b128 v[206:209], v156 offset:32768
	ds_read_b128 v[210:213], v156 offset:34816
	ds_read_b128 v[214:217], v155 offset:36864
	ds_read_b128 v[218:221], v155 offset:38912
	ds_read_b128 v[222:225], v156 offset:36864
	ds_read_b128 v[226:229], v156 offset:38912
	global_load_lds_dwordx4 v128, s[34:35]
	s_mov_b32 m0, s40
	s_nop 0
	global_load_lds_dwordx4 v130, s[34:35]
	s_waitcnt vmcnt(8)
	s_waitcnt lgkmcnt(0)
	s_barrier
	s_setprio 1
	s_waitcnt lgkmcnt(0)
	v_mfma_f32_16x16x32_f16 v[124:127], v[166:169], v[198:201], v[124:127]
	v_mfma_f32_16x16x32_f16 v[124:127], v[170:173], v[206:209], v[124:127]
	v_mfma_f32_16x16x32_f16 v[120:123], v[178:181], v[206:209], v[120:123]
	v_mfma_f32_16x16x32_f16 v[120:123], v[174:177], v[198:201], v[120:123]
	v_mfma_f32_16x16x32_f16 v[112:115], v[174:177], v[202:205], v[112:115]
	v_mfma_f32_16x16x32_f16 v[112:115], v[178:181], v[210:213], v[112:115]
	v_mfma_f32_16x16x32_f16 v[116:119], v[170:173], v[210:213], v[116:119]
	v_mfma_f32_16x16x32_f16 v[116:119], v[166:169], v[202:205], v[116:119]
	v_mfma_f32_16x16x32_f16 v[108:111], v[166:169], v[214:217], v[108:111]
	v_mfma_f32_16x16x32_f16 v[108:111], v[170:173], v[222:225], v[108:111]
	v_mfma_f32_16x16x32_f16 v[100:103], v[178:181], v[222:225], v[100:103]
	v_mfma_f32_16x16x32_f16 v[100:103], v[174:177], v[214:217], v[100:103]
	v_mfma_f32_16x16x32_f16 v[84:87], v[174:177], v[218:221], v[84:87]
	v_mfma_f32_16x16x32_f16 v[84:87], v[178:181], v[226:229], v[84:87]
	v_mfma_f32_16x16x32_f16 v[92:95], v[170:173], v[226:229], v[92:95]
	v_mfma_f32_16x16x32_f16 v[92:95], v[166:169], v[218:221], v[92:95]
	s_setprio 0
	s_setprio 1
	v_mfma_f32_16x16x32_f16 v[104:107], v[182:185], v[198:201], v[104:107]
	v_mfma_f32_16x16x32_f16 v[104:107], v[186:189], v[206:209], v[104:107]
	v_mfma_f32_16x16x32_f16 v[96:99], v[194:197], v[206:209], v[96:99]
	v_mfma_f32_16x16x32_f16 v[96:99], v[190:193], v[198:201], v[96:99]
	v_mfma_f32_16x16x32_f16 v[80:83], v[190:193], v[202:205], v[80:83]
	v_mfma_f32_16x16x32_f16 v[80:83], v[194:197], v[210:213], v[80:83]
	v_mfma_f32_16x16x32_f16 v[88:91], v[186:189], v[210:213], v[88:91]
	v_mfma_f32_16x16x32_f16 v[88:91], v[182:185], v[202:205], v[88:91]
	v_mfma_f32_16x16x32_f16 v[76:79], v[182:185], v[214:217], v[76:79]
	v_mfma_f32_16x16x32_f16 v[76:79], v[186:189], v[222:225], v[76:79]
	v_mfma_f32_16x16x32_f16 v[72:75], v[194:197], v[222:225], v[72:75]
	v_mfma_f32_16x16x32_f16 v[72:75], v[190:193], v[214:217], v[72:75]
	v_mfma_f32_16x16x32_f16 v[64:67], v[190:193], v[218:221], v[64:67]
	v_mfma_f32_16x16x32_f16 v[64:67], v[194:197], v[226:229], v[64:67]
	v_mfma_f32_16x16x32_f16 v[68:71], v[186:189], v[226:229], v[68:71]
	v_mfma_f32_16x16x32_f16 v[68:71], v[182:185], v[218:221], v[68:71]
	s_setprio 0
	s_barrier
	s_add_i32 s34, s46, s36
	s_mov_b32 m0, s34
	ds_read_b128 v[198:201], v155 offset:49152
	ds_read_b128 v[202:205], v155 offset:51200
	ds_read_b128 v[206:209], v156 offset:49152
	ds_read_b128 v[210:213], v156 offset:51200
	ds_read_b128 v[214:217], v155 offset:53248
	ds_read_b128 v[218:221], v155 offset:55296
	ds_read_b128 v[222:225], v156 offset:53248
	ds_read_b128 v[226:229], v156 offset:55296
	global_load_lds_dwordx4 v128, s[62:63]
	s_add_i32 m0, s34, 0x2000
	s_add_u32 s30, s30, 0x380080
	s_addc_u32 s31, s31, 0
	s_add_i32 s34, s47, s36
	global_load_lds_dwordx4 v130, s[62:63]
	s_mov_b32 m0, s34
	s_nop 0
	global_load_lds_dwordx4 v128, s[30:31]
	s_add_i32 m0, s34, 0x2000
	s_nop 0
	global_load_lds_dwordx4 v130, s[30:31]
	s_mov_b32 m0, s41
	s_nop 0
	global_load_lds_dwordx4 v128, s[64:65]
	s_mov_b32 m0, s42
	s_nop 0
	global_load_lds_dwordx4 v130, s[64:65]
	s_waitcnt vmcnt(8)
	s_waitcnt lgkmcnt(0)
	s_barrier
	s_setprio 1
	s_waitcnt lgkmcnt(0)
	v_mfma_f32_16x16x32_f16 v[60:63], v[166:169], v[198:201], v[60:63]
	v_mfma_f32_16x16x32_f16 v[60:63], v[170:173], v[206:209], v[60:63]
	v_mfma_f32_16x16x32_f16 v[56:59], v[178:181], v[206:209], v[56:59]
	v_mfma_f32_16x16x32_f16 v[56:59], v[174:177], v[198:201], v[56:59]
	v_mfma_f32_16x16x32_f16 v[48:51], v[174:177], v[202:205], v[48:51]
	v_mfma_f32_16x16x32_f16 v[48:51], v[178:181], v[210:213], v[48:51]
	v_mfma_f32_16x16x32_f16 v[52:55], v[170:173], v[210:213], v[52:55]
	v_mfma_f32_16x16x32_f16 v[52:55], v[166:169], v[202:205], v[52:55]
	v_mfma_f32_16x16x32_f16 v[40:43], v[166:169], v[214:217], v[40:43]
	v_mfma_f32_16x16x32_f16 v[40:43], v[170:173], v[222:225], v[40:43]
	v_mfma_f32_16x16x32_f16 v[32:35], v[178:181], v[222:225], v[32:35]
	v_mfma_f32_16x16x32_f16 v[32:35], v[174:177], v[214:217], v[32:35]
	v_mfma_f32_16x16x32_f16 v[8:11], v[174:177], v[218:221], v[8:11]
	v_mfma_f32_16x16x32_f16 v[8:11], v[178:181], v[226:229], v[8:11]
	v_mfma_f32_16x16x32_f16 v[12:15], v[170:173], v[226:229], v[12:15]
	v_mfma_f32_16x16x32_f16 v[12:15], v[166:169], v[218:221], v[12:15]
	s_setprio 0
	s_setprio 1
	v_mfma_f32_16x16x32_f16 v[44:47], v[182:185], v[198:201], v[44:47]
	v_mfma_f32_16x16x32_f16 v[44:47], v[186:189], v[206:209], v[44:47]
	v_mfma_f32_16x16x32_f16 v[36:39], v[194:197], v[206:209], v[36:39]
	v_mfma_f32_16x16x32_f16 v[36:39], v[190:193], v[198:201], v[36:39]
	v_mfma_f32_16x16x32_f16 v[24:27], v[190:193], v[202:205], v[24:27]
	v_mfma_f32_16x16x32_f16 v[24:27], v[194:197], v[210:213], v[24:27]
	v_mfma_f32_16x16x32_f16 v[28:31], v[186:189], v[210:213], v[28:31]
	v_mfma_f32_16x16x32_f16 v[28:31], v[182:185], v[202:205], v[28:31]
	v_mfma_f32_16x16x32_f16 v[20:23], v[182:185], v[214:217], v[20:23]
	v_mfma_f32_16x16x32_f16 v[20:23], v[186:189], v[222:225], v[20:23]
	v_mfma_f32_16x16x32_f16 v[16:19], v[194:197], v[222:225], v[16:19]
	v_mfma_f32_16x16x32_f16 v[16:19], v[190:193], v[214:217], v[16:19]
	v_mfma_f32_16x16x32_f16 v[0:3], v[190:193], v[218:221], v[0:3]
	v_mfma_f32_16x16x32_f16 v[0:3], v[194:197], v[226:229], v[0:3]
	v_mfma_f32_16x16x32_f16 v[4:7], v[186:189], v[226:229], v[4:7]
	v_mfma_f32_16x16x32_f16 v[4:7], v[182:185], v[218:221], v[4:7]
	s_setprio 0
	s_barrier
	s_add_i32 s58, s58, 2
	s_add_u32 s56, s56, 0x100
	s_addc_u32 s57, s57, 0
	s_add_u32 s28, s28, 0x100
	s_addc_u32 s29, s29, 0
	s_cmpk_gt_u32 s58, 0xdd
	s_cbranch_scc0 .LBB2_20
	v_lshl_add_u32 v144, s55, 8, v137
	v_ashrrev_i32_e32 v145, 31, v144
	v_lshl_add_u64 v[138:139], v[144:145], 2, s[10:11]
	global_load_dword v136, v[138:139], off
	global_load_dword v140, v[138:139], off offset:64
	global_load_dword v142, v[138:139], off offset:128
	global_load_dword v146, v[138:139], off offset:192
	global_load_dword v148, v[138:139], off offset:512
	global_load_dword v174, v[138:139], off offset:576
	global_load_dword v176, v[138:139], off offset:640
	s_nop 0
	global_load_dword v138, v[138:139], off offset:704
	v_lshl_or_b32 v166, s54, 8, v141
	v_ashrrev_i32_e32 v167, 31, v166
	v_or_b32_e32 v168, 16, v144
	v_or_b32_e32 v170, 32, v144
	v_or_b32_e32 v172, 48, v144
	v_lshl_add_u64 v[166:167], v[166:167], 2, s[8:9]
	v_lshlrev_b64 v[144:145], 14, v[144:145]
	v_ashrrev_i32_e32 v169, 31, v168
	v_ashrrev_i32_e32 v171, 31, v170
	v_ashrrev_i32_e32 v173, 31, v172
	v_lshl_add_u64 v[144:145], v[166:167], 0, v[144:145]
	v_lshlrev_b64 v[168:169], 14, v[168:169]
	v_lshlrev_b64 v[170:171], 14, v[170:171]
	v_lshlrev_b64 v[172:173], 14, v[172:173]
	v_add_co_u32_e32 v178, vcc, s48, v144
	v_lshl_add_u64 v[168:169], v[166:167], 0, v[168:169]
	v_lshl_add_u64 v[170:171], v[166:167], 0, v[170:171]
	v_lshl_add_u64 v[166:167], v[166:167], 0, v[172:173]
	v_lshl_add_u64 v[172:173], v[144:145], 0, s[16:17]
	v_addc_co_u32_e32 v179, vcc, 0, v145, vcc
	s_mov_b32 s55, s45
	s_mov_b32 s54, s53
	s_mov_b64 s[28:29], s[26:27]
	s_mov_b64 s[30:31], s[24:25]
	s_waitcnt vmcnt(0)
	v_pk_mul_f32 v[126:127], v[136:137], v[126:127] op_sel_hi:[0,1]
	v_pk_mul_f32 v[124:125], v[136:137], v[124:125] op_sel_hi:[0,1]
	v_pk_mul_f32 v[122:123], v[136:137], v[122:123] op_sel_hi:[0,1]
	v_pk_mul_f32 v[120:121], v[136:137], v[120:121] op_sel_hi:[0,1]
	v_pk_mul_f32 v[46:47], v[148:149], v[46:47] op_sel_hi:[0,1]
	v_pk_mul_f32 v[44:45], v[148:149], v[44:45] op_sel_hi:[0,1]
	v_pk_mul_f32 v[106:107], v[136:137], v[106:107] op_sel_hi:[0,1]
	v_pk_mul_f32 v[104:105], v[136:137], v[104:105] op_sel_hi:[0,1]
	v_pk_mul_f32 v[98:99], v[136:137], v[98:99] op_sel_hi:[0,1]
	v_pk_mul_f32 v[96:97], v[136:137], v[96:97] op_sel_hi:[0,1]
	v_pk_mul_f32 v[118:119], v[140:141], v[118:119] op_sel_hi:[0,1]
	v_pk_mul_f32 v[116:117], v[140:141], v[116:117] op_sel_hi:[0,1]
	v_pk_mul_f32 v[114:115], v[140:141], v[114:115] op_sel_hi:[0,1]
	v_pk_mul_f32 v[112:113], v[140:141], v[112:113] op_sel_hi:[0,1]
	v_pk_mul_f32 v[90:91], v[140:141], v[90:91] op_sel_hi:[0,1]
	v_pk_mul_f32 v[88:89], v[140:141], v[88:89] op_sel_hi:[0,1]
	v_pk_mul_f32 v[82:83], v[140:141], v[82:83] op_sel_hi:[0,1]
	v_pk_mul_f32 v[80:81], v[140:141], v[80:81] op_sel_hi:[0,1]
	v_pk_mul_f32 v[110:111], v[142:143], v[110:111] op_sel_hi:[0,1]
	v_pk_mul_f32 v[108:109], v[142:143], v[108:109] op_sel_hi:[0,1]
	v_pk_mul_f32 v[102:103], v[142:143], v[102:103] op_sel_hi:[0,1]
	v_pk_mul_f32 v[100:101], v[142:143], v[100:101] op_sel_hi:[0,1]
	v_pk_mul_f32 v[78:79], v[142:143], v[78:79] op_sel_hi:[0,1]
	v_pk_mul_f32 v[76:77], v[142:143], v[76:77] op_sel_hi:[0,1]
	v_pk_mul_f32 v[74:75], v[142:143], v[74:75] op_sel_hi:[0,1]
	v_pk_mul_f32 v[72:73], v[142:143], v[72:73] op_sel_hi:[0,1]
	v_pk_mul_f32 v[94:95], v[146:147], v[94:95] op_sel_hi:[0,1]
	v_pk_mul_f32 v[92:93], v[146:147], v[92:93] op_sel_hi:[0,1]
	v_pk_mul_f32 v[86:87], v[146:147], v[86:87] op_sel_hi:[0,1]
	v_pk_mul_f32 v[84:85], v[146:147], v[84:85] op_sel_hi:[0,1]
	v_pk_mul_f32 v[70:71], v[146:147], v[70:71] op_sel_hi:[0,1]
	v_pk_mul_f32 v[68:69], v[146:147], v[68:69] op_sel_hi:[0,1]
	v_pk_mul_f32 v[66:67], v[146:147], v[66:67] op_sel_hi:[0,1]
	v_pk_mul_f32 v[64:65], v[146:147], v[64:65] op_sel_hi:[0,1]
	v_pk_mul_f32 v[62:63], v[148:149], v[62:63] op_sel_hi:[0,1]
	v_pk_mul_f32 v[60:61], v[148:149], v[60:61] op_sel_hi:[0,1]
	global_store_dwordx4 v[144:145], v[124:127], off
	global_store_dwordx4 v[144:145], v[120:123], off offset:64
	global_store_dwordx4 v[144:145], v[104:107], off offset:512
	global_store_dwordx4 v[144:145], v[96:99], off offset:576
	global_store_dwordx4 v[168:169], v[116:119], off
	global_store_dwordx4 v[168:169], v[112:115], off offset:64
	global_store_dwordx4 v[168:169], v[88:91], off offset:512
	global_store_dwordx4 v[168:169], v[80:83], off offset:576
	global_store_dwordx4 v[170:171], v[108:111], off
	global_store_dwordx4 v[170:171], v[100:103], off offset:64
	global_store_dwordx4 v[170:171], v[76:79], off offset:512
	global_store_dwordx4 v[170:171], v[72:75], off offset:576
	global_store_dwordx4 v[166:167], v[92:95], off
	global_store_dwordx4 v[166:167], v[84:87], off offset:64
	global_store_dwordx4 v[166:167], v[68:71], off offset:512
	global_store_dwordx4 v[166:167], v[64:67], off offset:576
	global_store_dwordx4 v[178:179], v[60:63], off
	global_store_dwordx4 v[172:173], v[44:47], off offset:512
	v_pk_mul_f32 v[30:31], v[174:175], v[30:31] op_sel_hi:[0,1]
	v_pk_mul_f32 v[28:29], v[174:175], v[28:29] op_sel_hi:[0,1]
	v_add_co_u32_e32 v46, vcc, s49, v144
	v_lshl_add_u64 v[44:45], v[144:145], 0, s[18:19]
	s_nop 0
	v_addc_co_u32_e32 v47, vcc, 0, v145, vcc
	global_store_dwordx4 v[44:45], v[28:31], off offset:512
	v_pk_mul_f32 v[18:19], v[176:177], v[18:19] op_sel_hi:[0,1]
	v_pk_mul_f32 v[16:17], v[176:177], v[16:17] op_sel_hi:[0,1]
	v_add_co_u32_e32 v30, vcc, s50, v144
	v_lshl_add_u64 v[28:29], v[144:145], 0, s[20:21]
	s_nop 0
	v_addc_co_u32_e32 v31, vcc, 0, v145, vcc
	v_pk_mul_f32 v[38:39], v[148:149], v[38:39] op_sel_hi:[0,1]
	v_pk_mul_f32 v[36:37], v[148:149], v[36:37] op_sel_hi:[0,1]
	v_pk_mul_f32 v[26:27], v[174:175], v[26:27] op_sel_hi:[0,1]
	v_pk_mul_f32 v[24:25], v[174:175], v[24:25] op_sel_hi:[0,1]
	global_store_dwordx4 v[28:29], v[16:19], off offset:576
	global_store_dwordx4 v[172:173], v[36:39], off offset:576
	global_store_dwordx4 v[44:45], v[24:27], off offset:576
	v_add_co_u32_e32 v18, vcc, s51, v144
	v_pk_mul_f32 v[38:39], v[174:175], v[54:55] op_sel_hi:[0,1]
	v_pk_mul_f32 v[36:37], v[174:175], v[52:53] op_sel_hi:[0,1]
	v_pk_mul_f32 v[26:27], v[176:177], v[42:43] op_sel_hi:[0,1]
	v_pk_mul_f32 v[24:25], v[176:177], v[40:41] op_sel_hi:[0,1]
	v_addc_co_u32_e32 v19, vcc, 0, v145, vcc
	v_pk_mul_f32 v[58:59], v[148:149], v[58:59] op_sel_hi:[0,1]
	v_pk_mul_f32 v[56:57], v[148:149], v[56:57] op_sel_hi:[0,1]
	global_store_dwordx4 v[46:47], v[36:39], off
	global_store_dwordx4 v[30:31], v[24:27], off
	v_pk_mul_f32 v[22:23], v[176:177], v[22:23] op_sel_hi:[0,1]
	v_pk_mul_f32 v[38:39], v[174:175], v[50:51] op_sel_hi:[0,1]
	v_pk_mul_f32 v[36:37], v[174:175], v[48:49] op_sel_hi:[0,1]
	v_pk_mul_f32 v[26:27], v[176:177], v[34:35] op_sel_hi:[0,1]
	v_pk_mul_f32 v[24:25], v[176:177], v[32:33] op_sel_hi:[0,1]
	v_pk_mul_f32 v[20:21], v[176:177], v[20:21] op_sel_hi:[0,1]
	v_lshl_add_u64 v[16:17], v[144:145], 0, s[22:23]
	v_pk_mul_f32 v[14:15], v[138:139], v[14:15] op_sel_hi:[0,1]
	v_pk_mul_f32 v[12:13], v[138:139], v[12:13] op_sel_hi:[0,1]
	v_pk_mul_f32 v[10:11], v[138:139], v[10:11] op_sel_hi:[0,1]
	v_pk_mul_f32 v[8:9], v[138:139], v[8:9] op_sel_hi:[0,1]
	v_pk_mul_f32 v[6:7], v[138:139], v[6:7] op_sel_hi:[0,1]
	v_pk_mul_f32 v[4:5], v[138:139], v[4:5] op_sel_hi:[0,1]
	v_pk_mul_f32 v[2:3], v[138:139], v[2:3] op_sel_hi:[0,1]
	v_pk_mul_f32 v[0:1], v[138:139], v[0:1] op_sel_hi:[0,1]
	s_mov_b64 vcc, s[0:1]
	global_store_dwordx4 v[172:173], v[56:59], off offset:64
	global_store_dwordx4 v[44:45], v[36:39], off offset:64
	global_store_dwordx4 v[28:29], v[24:27], off offset:64
	global_store_dwordx4 v[28:29], v[20:23], off offset:512
	global_store_dwordx4 v[18:19], v[12:15], off
	global_store_dwordx4 v[16:17], v[8:11], off offset:64
	global_store_dwordx4 v[16:17], v[4:7], off offset:512
	global_store_dwordx4 v[16:17], v[0:3], off offset:576
	s_cbranch_vccz .LBB2_8
	s_waitcnt vmcnt(0)
	s_cmpk_gt_u32 s33, 0xff
	s_cbranch_scc1 .LBB2_24
	s_barrier

	.amdhsa_kernel _Z12gemm_persistILi1ELi14336ELi32ELi16EEvPKDF16_S1_PvPKfS4_S4_S4_PDF16_S5_iii
		.amdhsa_group_segment_fixed_size 0
		.amdhsa_private_segment_fixed_size 0
		.amdhsa_kernarg_size 344
		.amdhsa_user_sgpr_count 2
		.amdhsa_user_sgpr_dispatch_ptr 0
		.amdhsa_user_sgpr_queue_ptr 0
		.amdhsa_user_sgpr_kernarg_segment_ptr 1
		.amdhsa_user_sgpr_dispatch_id 0
		.amdhsa_user_sgpr_kernarg_preload_length 0
		.amdhsa_user_sgpr_kernarg_preload_offset 0
		.amdhsa_user_sgpr_private_segment_size 0
		.amdhsa_uses_dynamic_stack 0
		.amdhsa_enable_private_segment 0
		.amdhsa_system_sgpr_workgroup_id_x 1
		.amdhsa_system_sgpr_workgroup_id_y 0
		.amdhsa_system_sgpr_workgroup_id_z 0
		.amdhsa_system_sgpr_workgroup_info 0
		.amdhsa_system_vgpr_workitem_id 0
		.amdhsa_next_free_vgpr 236
		.amdhsa_next_free_sgpr 66
		.amdhsa_accum_offset 236
		.amdhsa_reserve_vcc 1
		.amdhsa_float_round_mode_32 0
		.amdhsa_float_round_mode_16_64 0
		.amdhsa_float_denorm_mode_32 3
		.amdhsa_float_denorm_mode_16_64 3
		.amdhsa_dx10_clamp 1
		.amdhsa_ieee_mode 1
		.amdhsa_fp16_overflow 0
		.amdhsa_tg_split 0
		.amdhsa_exception_fp_ieee_invalid_op 0
		.amdhsa_exception_fp_denorm_src 0
		.amdhsa_exception_fp_ieee_div_zero 0
		.amdhsa_exception_fp_ieee_overflow 0
		.amdhsa_exception_fp_ieee_underflow 0
		.amdhsa_exception_fp_ieee_inexact 0
		.amdhsa_exception_int_div_zero 0
	.end_amdhsa_kernel

amdhsa.kernels:
  - .agpr_count:     4
    .args:
      - .actual_access:  read_only
        .address_space:  global
        .offset:         0
        .size:           8
        .value_kind:     global_buffer
      - .actual_access:  read_only
        .address_space:  global
        .offset:         8
        .size:           8
        .value_kind:     global_buffer
      - .actual_access:  read_only
        .address_space:  global
        .offset:         16
        .size:           8
        .value_kind:     global_buffer
      - .actual_access:  read_only
        .address_space:  global
        .offset:         24
        .size:           8
        .value_kind:     global_buffer
      - .actual_access:  write_only
        .address_space:  global
        .offset:         32
        .size:           8
        .value_kind:     global_buffer
      - .actual_access:  write_only
        .address_space:  global
        .offset:         40
        .size:           8
        .value_kind:     global_buffer
      - .actual_access:  write_only
        .address_space:  global
        .offset:         48
        .size:           8
        .value_kind:     global_buffer
    .group_segment_fixed_size: 4352
    .kernarg_segment_align: 8
    .kernarg_segment_size: 56
    .language:       OpenCL C
    .language_version:
      - 2
      - 0
    .max_flat_workgroup_size: 256
    .name:           _Z11prep_kernelPKfS0_S0_S0_PDF16_PfS1_
    .private_segment_fixed_size: 0
    .sgpr_count:     26
    .sgpr_spill_count: 0
    .symbol:         _Z11prep_kernelPKfS0_S0_S0_PDF16_PfS1_.kd
    .uniform_work_group_size: 1
    .uses_dynamic_stack: false
    .vgpr_count:     56
    .vgpr_spill_count: 0
    .wavefront_size: 64
  - .agpr_count:     0
    .args:
      - .address_space:  global
        .offset:         0
        .size:           8
        .value_kind:     global_buffer
      - .address_space:  global
        .offset:         8
        .size:           8
        .value_kind:     global_buffer
      - .actual_access:  write_only
        .address_space:  global
        .offset:         16
        .size:           8
        .value_kind:     global_buffer
      - .actual_access:  read_only
        .address_space:  global
        .offset:         24
        .size:           8
        .value_kind:     global_buffer
      - .address_space:  global
        .offset:         32
        .size:           8
        .value_kind:     global_buffer
      - .address_space:  global
        .offset:         40
        .size:           8
        .value_kind:     global_buffer
      - .address_space:  global
        .offset:         48
        .size:           8
        .value_kind:     global_buffer
      - .actual_access:  write_only
        .address_space:  global
        .offset:         56
        .size:           8
        .value_kind:     global_buffer
      - .actual_access:  write_only
        .address_space:  global
        .offset:         64
        .size:           8
        .value_kind:     global_buffer
      - .offset:         72
        .size:           4
        .value_kind:     by_value
      - .offset:         76
        .size:           4
        .value_kind:     by_value
      - .offset:         80
        .size:           4
        .value_kind:     by_value
      - .offset:         88
        .size:           4
        .value_kind:     hidden_block_count_x
      - .offset:         92
        .size:           4
        .value_kind:     hidden_block_count_y
      - .offset:         96
        .size:           4
        .value_kind:     hidden_block_count_z
      - .offset:         100
        .size:           2
        .value_kind:     hidden_group_size_x
      - .offset:         102
        .size:           2
        .value_kind:     hidden_group_size_y
      - .offset:         104
        .size:           2
        .value_kind:     hidden_group_size_z
      - .offset:         106
        .size:           2
        .value_kind:     hidden_remainder_x
      - .offset:         108
        .size:           2
        .value_kind:     hidden_remainder_y
      - .offset:         110
        .size:           2
        .value_kind:     hidden_remainder_z
      - .offset:         128
        .size:           8
        .value_kind:     hidden_global_offset_x
      - .offset:         136
        .size:           8
        .value_kind:     hidden_global_offset_y
      - .offset:         144
        .size:           8
        .value_kind:     hidden_global_offset_z
      - .offset:         152
        .size:           2
        .value_kind:     hidden_grid_dims
      - .offset:         208
        .size:           4
        .value_kind:     hidden_dynamic_lds_size
    .group_segment_fixed_size: 0
    .kernarg_segment_align: 8
    .kernarg_segment_size: 344
    .language:       OpenCL C
    .language_version:
      - 2
      - 0
    .max_flat_workgroup_size: 512
    .name:           _Z12gemm_persistILi0ELi4096ELi32ELi112EEvPKDF16_S1_PvPKfS4_S4_S4_PDF16_S5_iii
    .private_segment_fixed_size: 0
    .sgpr_count:     94
    .sgpr_spill_count: 0
    .symbol:         _Z12gemm_persistILi0ELi4096ELi32ELi112EEvPKDF16_S1_PvPKfS4_S4_S4_PDF16_S5_iii.kd
    .uniform_work_group_size: 1
    .uses_dynamic_stack: false
    .vgpr_count:     232
    .vgpr_spill_count: 0
    .wavefront_size: 64
  - .agpr_count:     0
    .args:
      - .address_space:  global
        .offset:         0
        .size:           8
        .value_kind:     global_buffer
      - .address_space:  global
        .offset:         8
        .size:           8
        .value_kind:     global_buffer
      - .actual_access:  write_only
        .address_space:  global
        .offset:         16
        .size:           8
        .value_kind:     global_buffer
      - .actual_access:  read_only
        .address_space:  global
        .offset:         24
        .size:           8
        .value_kind:     global_buffer
      - .actual_access:  read_only
        .address_space:  global
        .offset:         32
        .size:           8
        .value_kind:     global_buffer
      - .actual_access:  read_only
        .address_space:  global
        .offset:         40
        .size:           8
        .value_kind:     global_buffer
      - .actual_access:  read_only
        .address_space:  global
        .offset:         48
        .size:           8
        .value_kind:     global_buffer
      - .actual_access:  read_only
        .address_space:  global
        .offset:         56
        .size:           8
        .value_kind:     global_buffer
      - .actual_access:  read_only
        .address_space:  global
        .offset:         64
        .size:           8
        .value_kind:     global_buffer
      - .offset:         72
        .size:           4
        .value_kind:     by_value
      - .offset:         76
        .size:           4
        .value_kind:     by_value
      - .offset:         80
        .size:           4
        .value_kind:     by_value
      - .offset:         88
        .size:           4
        .value_kind:     hidden_block_count_x
      - .offset:         92
        .size:           4
        .value_kind:     hidden_block_count_y
      - .offset:         96
        .size:           4
        .value_kind:     hidden_block_count_z
      - .offset:         100
        .size:           2
        .value_kind:     hidden_group_size_x
      - .offset:         102
        .size:           2
        .value_kind:     hidden_group_size_y
      - .offset:         104
        .size:           2
        .value_kind:     hidden_group_size_z
      - .offset:         106
        .size:           2
        .value_kind:     hidden_remainder_x
      - .offset:         108
        .size:           2
        .value_kind:     hidden_remainder_y
      - .offset:         110
        .size:           2
        .value_kind:     hidden_remainder_z
      - .offset:         128
        .size:           8
        .value_kind:     hidden_global_offset_x
      - .offset:         136
        .size:           8
        .value_kind:     hidden_global_offset_y
      - .offset:         144
        .size:           8
        .value_kind:     hidden_global_offset_z
      - .offset:         152
        .size:           2
        .value_kind:     hidden_grid_dims
      - .offset:         208
        .size:           4
        .value_kind:     hidden_dynamic_lds_size
    .group_segment_fixed_size: 0
    .kernarg_segment_align: 8
    .kernarg_segment_size: 344
    .language:       OpenCL C
    .language_version:
      - 2
      - 0
    .max_flat_workgroup_size: 512
    .name:           _Z12gemm_persistILi1ELi14336ELi32ELi16EEvPKDF16_S1_PvPKfS4_S4_S4_PDF16_S5_iii
    .private_segment_fixed_size: 0
    .sgpr_count:     72
    .sgpr_spill_count: 0
    .symbol:         _Z12gemm_persistILi1ELi14336ELi32ELi16EEvPKDF16_S1_PvPKfS4_S4_S4_PDF16_S5_iii.kd
    .uniform_work_group_size: 1
    .uses_dynamic_stack: false
    .vgpr_count:     236
    .vgpr_spill_count: 0
    .wavefront_size: 64
